# combo9 + P0 forget-gate weight columns: four row loads issued together, one wait, 16 stores (was four load->vmcnt(0)->4 stores rounds on P0's critical path)
# speedup vs baseline: 1.0096x; 1.0096x over previous
.LBB0_64:
	global_load_dwordx4 v[6:9], v[4:5], off
	global_load_dwordx4 v[18:21], v[4:5], off offset:16
	global_load_dwordx4 v[22:25], v[4:5], off offset:32
	global_load_dwordx4 v[26:29], v[4:5], off offset:48
	v_add_u32_e32 v0, s6, v0
	v_cmp_lt_i32_e32 vcc, s0, v0
	s_or_b64 s[12:13], vcc, s[12:13]
	s_mov_b32 s73, 0
	s_waitcnt vmcnt(0)
	s_mov_b32 s72, 0x0
	v_lshl_add_u64 v[10:11], v[2:3], 0, s[72:73]
	v_cvt_pk_bf16_f32 v30, v6, v1
	global_store_short v[10:11], v30, off
	s_mov_b32 s72, 0x2000
	v_lshl_add_u64 v[12:13], v[2:3], 0, s[72:73]
	v_cvt_pk_bf16_f32 v31, v7, v1
	global_store_short v[12:13], v31, off
	s_mov_b32 s72, 0x4000
	v_lshl_add_u64 v[14:15], v[2:3], 0, s[72:73]
	v_cvt_pk_bf16_f32 v30, v8, v1
	global_store_short v[14:15], v30, off
	s_mov_b32 s72, 0x6000
	v_lshl_add_u64 v[16:17], v[2:3], 0, s[72:73]
	v_cvt_pk_bf16_f32 v31, v9, v1
	global_store_short v[16:17], v31, off
	s_mov_b32 s72, 0x8000
	v_lshl_add_u64 v[10:11], v[2:3], 0, s[72:73]
	v_cvt_pk_bf16_f32 v30, v18, v1
	global_store_short v[10:11], v30, off
	s_mov_b32 s72, 0xa000
	v_lshl_add_u64 v[12:13], v[2:3], 0, s[72:73]
	v_cvt_pk_bf16_f32 v31, v19, v1
	global_store_short v[12:13], v31, off
	s_mov_b32 s72, 0xc000
	v_lshl_add_u64 v[14:15], v[2:3], 0, s[72:73]
	v_cvt_pk_bf16_f32 v30, v20, v1
	global_store_short v[14:15], v30, off
	s_mov_b32 s72, 0xe000
	v_lshl_add_u64 v[16:17], v[2:3], 0, s[72:73]
	v_cvt_pk_bf16_f32 v31, v21, v1
	global_store_short v[16:17], v31, off
	s_mov_b32 s72, 0x10000
	v_lshl_add_u64 v[10:11], v[2:3], 0, s[72:73]
	v_cvt_pk_bf16_f32 v30, v22, v1
	global_store_short v[10:11], v30, off
	s_mov_b32 s72, 0x12000
	v_lshl_add_u64 v[12:13], v[2:3], 0, s[72:73]
	v_cvt_pk_bf16_f32 v31, v23, v1
	global_store_short v[12:13], v31, off
	s_mov_b32 s72, 0x14000
	v_lshl_add_u64 v[14:15], v[2:3], 0, s[72:73]
	v_cvt_pk_bf16_f32 v30, v24, v1
	global_store_short v[14:15], v30, off
	s_mov_b32 s72, 0x16000
	v_lshl_add_u64 v[16:17], v[2:3], 0, s[72:73]
	v_cvt_pk_bf16_f32 v31, v25, v1
	global_store_short v[16:17], v31, off
	s_mov_b32 s72, 0x18000
	v_lshl_add_u64 v[10:11], v[2:3], 0, s[72:73]
	v_cvt_pk_bf16_f32 v30, v26, v1
	global_store_short v[10:11], v30, off
	s_mov_b32 s72, 0x1a000
	v_lshl_add_u64 v[12:13], v[2:3], 0, s[72:73]
	v_cvt_pk_bf16_f32 v31, v27, v1
	global_store_short v[12:13], v31, off
	s_mov_b32 s72, 0x1c000
	v_lshl_add_u64 v[14:15], v[2:3], 0, s[72:73]
	v_cvt_pk_bf16_f32 v30, v28, v1
	global_store_short v[14:15], v30, off
	s_mov_b32 s72, 0x1e000
	v_lshl_add_u64 v[16:17], v[2:3], 0, s[72:73]
	v_cvt_pk_bf16_f32 v31, v29, v1
	global_store_short v[16:17], v31, off
	v_lshl_add_u64 v[4:5], v[4:5], 0, s[10:11]
	v_lshl_add_u64 v[2:3], v[2:3], 0, s[8:9]
	s_andn2_b64 exec, exec, s[12:13]
	s_cbranch_execnz .LBB0_64
